# baseline (speedup 1.0000x reference)
.LBB0_21:
	v_exp_f32_e64 v156, -|v154|
	v_max_f32 v157, 0, v154
	v_add_f32 v156, 1.0, v156
	v_log_f32 v156, v156
	s_nop 0
	v_fma_mixlo_f16 v155, v156, 1.0, v157
	ds_write_b16 v148, v155
	v_mov_b32_e32 v192, v106
	v_mov_b32_e32 v193, v110
	v_mul_f32 v182, -2.0, v153
	s_nop 6
	ds_read_b128 v[208:211], v139
	s_waitcnt lgkmcnt(1)
	s_barrier
	ds_read_b128 v[212:215], v140
	ds_read_b128 v[216:219], v141
	s_waitcnt lgkmcnt(2)
	v_smfmac_f32_16x16x64_f16 v[192:195], v[208:211], v[6:13], v191
	ds_read_b128 v[220:223], v142
	s_waitcnt lgkmcnt(2)
	v_smfmac_f32_16x16x64_f16 v[192:195], v[212:215], v[14:21], v191
	s_waitcnt lgkmcnt(1)
	v_smfmac_f32_16x16x64_f16 v[192:195], v[216:219], v[26:33], v191
	s_waitcnt lgkmcnt(0)
	v_smfmac_f32_16x16x64_f16 v[192:195], v[220:223], v[34:41], v191
	s_nop 7
	v_cndmask_b32_e64 v154, v192, v193, s[0:1]
	v_exp_f32_e64 v156, -|v154|
	v_max_f32 v157, 0, v154
	v_add_f32 v156, 1.0, v156
	v_log_f32 v156, v156
	s_nop 0
	v_fma_mixlo_f16 v155, v156, 1.0, v157
	ds_write_b16 v149, v155
	v_mov_b32_e32 v200, v114
	v_mov_b32_e32 v201, v118
	v_mov_b32_e32 v204, v122
	v_mov_b32_e32 v205, v126
	s_nop 3
	ds_read_b128 v[208:211], v143
	s_waitcnt lgkmcnt(1)
	s_barrier
	ds_read_b128 v[212:215], v144
	ds_read_b128 v[216:219], v145
	s_waitcnt lgkmcnt(2)
	v_smfmac_f32_16x16x64_f16 v[200:203], v[208:211], v[42:49], v191
	v_smfmac_f32_16x16x64_f16 v[204:207], v[208:211], v[74:81], v191
	ds_read_b128 v[220:223], v146
	s_waitcnt lgkmcnt(2)
	v_smfmac_f32_16x16x64_f16 v[200:203], v[212:215], v[50:57], v191
	v_smfmac_f32_16x16x64_f16 v[204:207], v[212:215], v[82:89], v191
	s_waitcnt lgkmcnt(1)
	v_smfmac_f32_16x16x64_f16 v[200:203], v[216:219], v[58:65], v191
	v_smfmac_f32_16x16x64_f16 v[204:207], v[216:219], v[90:97], v191
	s_waitcnt lgkmcnt(0)
	v_smfmac_f32_16x16x64_f16 v[200:203], v[220:223], v[66:73], v191
	v_smfmac_f32_16x16x64_f16 v[204:207], v[220:223], v[98:105], v191
	s_nop 6
	v_cndmask_b32_e64 v170, v201, v200, s[6:7]
	v_cndmask_b32_e64 v170, v170, v204, s[0:1]
	v_cndmask_b32_e64 v170, v170, v205, s[4:5]
	v_exp_f32_e32 v170, v170
	s_nop 0
	v_add_f32_e32 v170, 1.0, v170
	v_rcp_f32_e32 v170, v170
	s_nop 0
	v_fmac_f32_e32 v153, v170, v182
	s_nop 1
	v_add_f32_dpp v153, v153, v153 quad_perm:[1,0,3,2] row_mask:0xf bank_mask:0xf bound_ctrl:1
	s_nop 1
	v_add_f32_dpp v153, v153, v153 quad_perm:[2,3,0,1] row_mask:0xf bank_mask:0xf bound_ctrl:1
	s_nop 1
	v_add_f32_dpp v153, v153, v153 row_half_mirror row_mask:0xf bank_mask:0xf bound_ctrl:1
	v_cvt_f16_f32_e32 v170, v153
	ds_write_b16 v150, v170
	s_waitcnt lgkmcnt(0)
	s_barrier
	ds_read_b128 v[154:157], v147
	s_waitcnt lgkmcnt(0)
	v_smfmac_f32_16x16x64_f16 v[130:133], v[154:157], v[248:255], v191
	s_nop 2
	v_add_u32_e32 v134, s3, v151
	ds_read_b32 v135, v134
	s_nop 2
	v_cndmask_b32_e64 v136, v130, v131, s[0:1]
	v_exp_f32_e64 v158, -|v136|
	v_max_f32 v159, 0, v136
	v_add_f32 v158, 1.0, v158
	v_log_f32 v158, v158
	s_nop 0
	v_fma_mixlo_f16 v137, v158, 1.0, v159
	ds_write_b16 v148, v137
	v_mov_b32_e32 v192, v106
	v_mov_b32_e32 v193, v110
	v_add_f32_e32 v136, v152, v153
	v_mul_f32 v137, -2.0, v135
	s_nop 6
	ds_read_b128 v[208:211], v139
	s_waitcnt lgkmcnt(1)
	s_barrier
	ds_read_b128 v[212:215], v140
	ds_read_b128 v[216:219], v141
	s_waitcnt lgkmcnt(2)
	v_smfmac_f32_16x16x64_f16 v[192:195], v[208:211], v[6:13], v191
	ds_read_b128 v[220:223], v142
	s_waitcnt lgkmcnt(2)
	v_smfmac_f32_16x16x64_f16 v[192:195], v[212:215], v[14:21], v191
	s_waitcnt lgkmcnt(1)
	v_smfmac_f32_16x16x64_f16 v[192:195], v[216:219], v[26:33], v191
	s_waitcnt lgkmcnt(0)
	v_smfmac_f32_16x16x64_f16 v[192:195], v[220:223], v[34:41], v191
	s_nop 7
	v_cndmask_b32_e64 v152, v192, v193, s[0:1]
	v_exp_f32_e64 v158, -|v152|
	v_max_f32 v159, 0, v152
	v_add_f32 v158, 1.0, v158
	v_log_f32 v158, v158
	s_nop 0
	v_fma_mixlo_f16 v153, v158, 1.0, v159
	ds_write_b16 v149, v153
	v_mov_b32_e32 v200, v114
	v_mov_b32_e32 v201, v118
	v_mov_b32_e32 v204, v122
	v_mov_b32_e32 v205, v126
	s_nop 3
	ds_read_b128 v[208:211], v143
	s_waitcnt lgkmcnt(1)
	s_barrier
	ds_read_b128 v[212:215], v144
	ds_read_b128 v[216:219], v145
	s_waitcnt lgkmcnt(2)
	v_smfmac_f32_16x16x64_f16 v[200:203], v[208:211], v[42:49], v191
	v_smfmac_f32_16x16x64_f16 v[204:207], v[208:211], v[74:81], v191
	ds_read_b128 v[220:223], v146
	s_waitcnt lgkmcnt(2)
	v_smfmac_f32_16x16x64_f16 v[200:203], v[212:215], v[50:57], v191
	v_smfmac_f32_16x16x64_f16 v[204:207], v[212:215], v[82:89], v191
	s_waitcnt lgkmcnt(1)
	v_smfmac_f32_16x16x64_f16 v[200:203], v[216:219], v[58:65], v191
	v_smfmac_f32_16x16x64_f16 v[204:207], v[216:219], v[90:97], v191
	s_waitcnt lgkmcnt(0)
	v_smfmac_f32_16x16x64_f16 v[200:203], v[220:223], v[66:73], v191
	v_smfmac_f32_16x16x64_f16 v[204:207], v[220:223], v[98:105], v191
	s_nop 6
	v_cndmask_b32_e64 v152, v201, v200, s[6:7]
	v_cndmask_b32_e64 v152, v152, v204, s[0:1]
	v_cndmask_b32_e64 v152, v152, v205, s[4:5]
	v_exp_f32_e32 v152, v152
	s_nop 0
	v_add_f32_e32 v152, 1.0, v152
	v_rcp_f32_e32 v152, v152
	s_nop 0
	v_fmac_f32_e32 v135, v152, v137
	s_nop 1
	v_add_f32_dpp v135, v135, v135 quad_perm:[1,0,3,2] row_mask:0xf bank_mask:0xf bound_ctrl:1
	s_nop 1
	v_add_f32_dpp v135, v135, v135 quad_perm:[2,3,0,1] row_mask:0xf bank_mask:0xf bound_ctrl:1
	s_nop 1
	v_add_f32_dpp v135, v135, v135 row_half_mirror row_mask:0xf bank_mask:0xf bound_ctrl:1
	v_cvt_f16_f32_e32 v137, v135
	ds_write_b16 v150, v137
	s_waitcnt lgkmcnt(0)
	s_barrier
	ds_read_b128 v[158:161], v147
	s_nop 3
	ds_read_b32 v137, v134 offset:32
	v_add_f32_e32 v135, v136, v135
	s_waitcnt lgkmcnt(1)
	v_smfmac_f32_16x16x64_f16 v[130:133], v[158:161], v[248:255], v191
	s_nop 7
	v_cndmask_b32_e64 v156, v130, v131, s[0:1]
	v_exp_f32_e64 v158, -|v156|
	v_max_f32 v159, 0, v156
	v_add_f32 v158, 1.0, v158
	v_log_f32 v158, v158
	s_nop 0
	v_fma_mixlo_f16 v157, v158, 1.0, v159
	ds_write_b16 v148, v157
	v_mov_b32_e32 v192, v106
	v_mov_b32_e32 v193, v110
	v_mul_f32 v136, -2.0, v137
	s_nop 6
	ds_read_b128 v[208:211], v139
	s_waitcnt lgkmcnt(1)
	s_barrier
	ds_read_b128 v[212:215], v140
	ds_read_b128 v[216:219], v141
	s_waitcnt lgkmcnt(2)
	v_smfmac_f32_16x16x64_f16 v[192:195], v[208:211], v[6:13], v191
	ds_read_b128 v[220:223], v142
	s_waitcnt lgkmcnt(2)
	v_smfmac_f32_16x16x64_f16 v[192:195], v[212:215], v[14:21], v191
	s_waitcnt lgkmcnt(1)
	v_smfmac_f32_16x16x64_f16 v[192:195], v[216:219], v[26:33], v191
	s_waitcnt lgkmcnt(0)
	v_smfmac_f32_16x16x64_f16 v[192:195], v[220:223], v[34:41], v191
	s_nop 7
	v_cndmask_b32_e64 v156, v192, v193, s[0:1]
	v_exp_f32_e64 v158, -|v156|
	v_max_f32 v159, 0, v156
	v_add_f32 v158, 1.0, v158
	v_log_f32 v158, v158
	s_nop 0
	v_fma_mixlo_f16 v157, v158, 1.0, v159
	ds_write_b16 v149, v157
	v_mov_b32_e32 v200, v114
	v_mov_b32_e32 v201, v118
	v_mov_b32_e32 v204, v122
	v_mov_b32_e32 v205, v126
	s_nop 3
	ds_read_b128 v[208:211], v143
	s_waitcnt lgkmcnt(1)
	s_barrier
	ds_read_b128 v[212:215], v144
	ds_read_b128 v[216:219], v145
	s_waitcnt lgkmcnt(2)
	v_smfmac_f32_16x16x64_f16 v[200:203], v[208:211], v[42:49], v191
	v_smfmac_f32_16x16x64_f16 v[204:207], v[208:211], v[74:81], v191
	ds_read_b128 v[220:223], v146
	s_waitcnt lgkmcnt(2)
	v_smfmac_f32_16x16x64_f16 v[200:203], v[212:215], v[50:57], v191
	v_smfmac_f32_16x16x64_f16 v[204:207], v[212:215], v[82:89], v191
	s_waitcnt lgkmcnt(1)
	v_smfmac_f32_16x16x64_f16 v[200:203], v[216:219], v[58:65], v191
	v_smfmac_f32_16x16x64_f16 v[204:207], v[216:219], v[90:97], v191
	s_waitcnt lgkmcnt(0)
	v_smfmac_f32_16x16x64_f16 v[200:203], v[220:223], v[66:73], v191
	v_smfmac_f32_16x16x64_f16 v[204:207], v[220:223], v[98:105], v191
	s_nop 6
	v_cndmask_b32_e64 v172, v201, v200, s[6:7]
	v_cndmask_b32_e64 v172, v172, v204, s[0:1]
	v_cndmask_b32_e64 v172, v172, v205, s[4:5]
	v_exp_f32_e32 v172, v172
	s_nop 0
	v_add_f32_e32 v172, 1.0, v172
	v_rcp_f32_e32 v172, v172
	s_nop 0
	v_fmac_f32_e32 v137, v172, v136
	s_nop 1
	v_add_f32_dpp v136, v137, v137 quad_perm:[1,0,3,2] row_mask:0xf bank_mask:0xf bound_ctrl:1
	s_nop 1
	v_add_f32_dpp v136, v136, v136 quad_perm:[2,3,0,1] row_mask:0xf bank_mask:0xf bound_ctrl:1
	s_nop 1
	v_add_f32_dpp v136, v136, v136 row_half_mirror row_mask:0xf bank_mask:0xf bound_ctrl:1
	v_cvt_f16_f32_e32 v137, v136
	ds_write_b16 v150, v137
	s_waitcnt lgkmcnt(0)
	s_barrier
	ds_read_b128 v[156:159], v147
	s_nop 3
	ds_read_b32 v137, v134 offset:64
	v_add_f32_e32 v135, v135, v136
	s_waitcnt lgkmcnt(1)
	v_smfmac_f32_16x16x64_f16 v[130:133], v[156:159], v[248:255], v191
	s_nop 7
	v_cndmask_b32_e64 v156, v130, v131, s[0:1]
	v_exp_f32_e64 v158, -|v156|
	v_max_f32 v159, 0, v156
	v_add_f32 v158, 1.0, v158
	v_log_f32 v158, v158
	s_nop 0
	v_fma_mixlo_f16 v157, v158, 1.0, v159
	ds_write_b16 v148, v157
	v_mov_b32_e32 v192, v106
	v_mov_b32_e32 v193, v110
	v_mul_f32 v136, -2.0, v137
	s_nop 6
	ds_read_b128 v[208:211], v139
	s_waitcnt lgkmcnt(1)
	s_barrier
	ds_read_b128 v[212:215], v140
	ds_read_b128 v[216:219], v141
	s_waitcnt lgkmcnt(2)
	v_smfmac_f32_16x16x64_f16 v[192:195], v[208:211], v[6:13], v191
	ds_read_b128 v[220:223], v142
	s_waitcnt lgkmcnt(2)
	v_smfmac_f32_16x16x64_f16 v[192:195], v[212:215], v[14:21], v191
	s_waitcnt lgkmcnt(1)
	v_smfmac_f32_16x16x64_f16 v[192:195], v[216:219], v[26:33], v191
	s_waitcnt lgkmcnt(0)
	v_smfmac_f32_16x16x64_f16 v[192:195], v[220:223], v[34:41], v191
	s_nop 7
	v_cndmask_b32_e64 v156, v192, v193, s[0:1]
	v_exp_f32_e64 v158, -|v156|
	v_max_f32 v159, 0, v156
	v_add_f32 v158, 1.0, v158
	v_log_f32 v158, v158
	s_nop 0
	v_fma_mixlo_f16 v157, v158, 1.0, v159
	ds_write_b16 v149, v157
	v_mov_b32_e32 v200, v114
	v_mov_b32_e32 v201, v118
	v_mov_b32_e32 v204, v122
	v_mov_b32_e32 v205, v126
	s_nop 3
	ds_read_b128 v[208:211], v143
	s_waitcnt lgkmcnt(1)
	s_barrier
	ds_read_b128 v[212:215], v144
	ds_read_b128 v[216:219], v145
	s_waitcnt lgkmcnt(2)
	v_smfmac_f32_16x16x64_f16 v[200:203], v[208:211], v[42:49], v191
	v_smfmac_f32_16x16x64_f16 v[204:207], v[208:211], v[74:81], v191
	ds_read_b128 v[220:223], v146
	s_waitcnt lgkmcnt(2)
	v_smfmac_f32_16x16x64_f16 v[200:203], v[212:215], v[50:57], v191
	v_smfmac_f32_16x16x64_f16 v[204:207], v[212:215], v[82:89], v191
	s_waitcnt lgkmcnt(1)
	v_smfmac_f32_16x16x64_f16 v[200:203], v[216:219], v[58:65], v191
	v_smfmac_f32_16x16x64_f16 v[204:207], v[216:219], v[90:97], v191
	s_waitcnt lgkmcnt(0)
	v_smfmac_f32_16x16x64_f16 v[200:203], v[220:223], v[66:73], v191
	v_smfmac_f32_16x16x64_f16 v[204:207], v[220:223], v[98:105], v191
	s_nop 6
	v_cndmask_b32_e64 v172, v201, v200, s[6:7]
	v_cndmask_b32_e64 v172, v172, v204, s[0:1]
	v_cndmask_b32_e64 v172, v172, v205, s[4:5]
	v_exp_f32_e32 v172, v172
	s_nop 0
	v_add_f32_e32 v172, 1.0, v172
	v_rcp_f32_e32 v172, v172
	s_nop 0
	v_fmac_f32_e32 v137, v172, v136
	s_nop 1
	v_add_f32_dpp v136, v137, v137 quad_perm:[1,0,3,2] row_mask:0xf bank_mask:0xf bound_ctrl:1
	s_nop 1
	v_add_f32_dpp v136, v136, v136 quad_perm:[2,3,0,1] row_mask:0xf bank_mask:0xf bound_ctrl:1
	s_nop 1
	v_add_f32_dpp v136, v136, v136 row_half_mirror row_mask:0xf bank_mask:0xf bound_ctrl:1
	v_cvt_f16_f32_e32 v137, v136
	ds_write_b16 v150, v137
	s_waitcnt lgkmcnt(0)
	s_barrier
	ds_read_b128 v[156:159], v147
	s_nop 3
	ds_read_b32 v137, v134 offset:96
	v_add_f32_e32 v135, v135, v136
	s_waitcnt lgkmcnt(1)
	v_smfmac_f32_16x16x64_f16 v[130:133], v[156:159], v[248:255], v191
	s_nop 7
	v_cndmask_b32_e64 v156, v130, v131, s[0:1]
	v_exp_f32_e64 v158, -|v156|
	v_max_f32 v159, 0, v156
	v_add_f32 v158, 1.0, v158
	v_log_f32 v158, v158
	s_nop 0
	v_fma_mixlo_f16 v157, v158, 1.0, v159
	ds_write_b16 v148, v157
	v_mov_b32_e32 v192, v106
	v_mov_b32_e32 v193, v110
	v_mul_f32 v136, -2.0, v137
	s_nop 6
	ds_read_b128 v[208:211], v139
	s_waitcnt lgkmcnt(1)
	s_barrier
	ds_read_b128 v[212:215], v140
	ds_read_b128 v[216:219], v141
	s_waitcnt lgkmcnt(2)
	v_smfmac_f32_16x16x64_f16 v[192:195], v[208:211], v[6:13], v191
	ds_read_b128 v[220:223], v142
	s_waitcnt lgkmcnt(2)
	v_smfmac_f32_16x16x64_f16 v[192:195], v[212:215], v[14:21], v191
	s_waitcnt lgkmcnt(1)
	v_smfmac_f32_16x16x64_f16 v[192:195], v[216:219], v[26:33], v191
	s_waitcnt lgkmcnt(0)
	v_smfmac_f32_16x16x64_f16 v[192:195], v[220:223], v[34:41], v191
	s_nop 7
	v_cndmask_b32_e64 v156, v192, v193, s[0:1]
	v_exp_f32_e64 v158, -|v156|
	v_max_f32 v159, 0, v156
	v_add_f32 v158, 1.0, v158
	v_log_f32 v158, v158
	s_nop 0
	v_fma_mixlo_f16 v157, v158, 1.0, v159
	ds_write_b16 v149, v157
	v_mov_b32_e32 v200, v114
	v_mov_b32_e32 v201, v118
	v_mov_b32_e32 v204, v122
	v_mov_b32_e32 v205, v126
	s_nop 3
	ds_read_b128 v[208:211], v143
	s_waitcnt lgkmcnt(1)
	s_barrier
	ds_read_b128 v[212:215], v144
	ds_read_b128 v[216:219], v145
	s_waitcnt lgkmcnt(2)
	v_smfmac_f32_16x16x64_f16 v[200:203], v[208:211], v[42:49], v191
	v_smfmac_f32_16x16x64_f16 v[204:207], v[208:211], v[74:81], v191
	ds_read_b128 v[220:223], v146
	s_waitcnt lgkmcnt(2)
	v_smfmac_f32_16x16x64_f16 v[200:203], v[212:215], v[50:57], v191
	v_smfmac_f32_16x16x64_f16 v[204:207], v[212:215], v[82:89], v191
	s_waitcnt lgkmcnt(1)
	v_smfmac_f32_16x16x64_f16 v[200:203], v[216:219], v[58:65], v191
	v_smfmac_f32_16x16x64_f16 v[204:207], v[216:219], v[90:97], v191
	s_waitcnt lgkmcnt(0)
	v_smfmac_f32_16x16x64_f16 v[200:203], v[220:223], v[66:73], v191
	v_smfmac_f32_16x16x64_f16 v[204:207], v[220:223], v[98:105], v191
	s_nop 6
	v_cndmask_b32_e64 v172, v201, v200, s[6:7]
	v_cndmask_b32_e64 v172, v172, v204, s[0:1]
	v_cndmask_b32_e64 v172, v172, v205, s[4:5]
	v_exp_f32_e32 v172, v172
	s_nop 0
	v_add_f32_e32 v172, 1.0, v172
	v_rcp_f32_e32 v172, v172
	s_nop 0
	v_fmac_f32_e32 v137, v172, v136
	s_nop 1
	v_add_f32_dpp v136, v137, v137 quad_perm:[1,0,3,2] row_mask:0xf bank_mask:0xf bound_ctrl:1
	s_nop 1
	v_add_f32_dpp v136, v136, v136 quad_perm:[2,3,0,1] row_mask:0xf bank_mask:0xf bound_ctrl:1
	s_nop 1
	v_add_f32_dpp v136, v136, v136 row_half_mirror row_mask:0xf bank_mask:0xf bound_ctrl:1
	v_cvt_f16_f32_e32 v137, v136
	ds_write_b16 v150, v137
	s_waitcnt lgkmcnt(0)
	s_barrier
	ds_read_b128 v[156:159], v147
	s_nop 3
	ds_read_b32 v137, v134 offset:128
	v_add_f32_e32 v135, v135, v136
	s_waitcnt lgkmcnt(1)
	v_smfmac_f32_16x16x64_f16 v[130:133], v[156:159], v[248:255], v191
	s_nop 7
	v_cndmask_b32_e64 v156, v130, v131, s[0:1]
	v_exp_f32_e64 v158, -|v156|
	v_max_f32 v159, 0, v156
	v_add_f32 v158, 1.0, v158
	v_log_f32 v158, v158
	s_nop 0
	v_fma_mixlo_f16 v157, v158, 1.0, v159
	ds_write_b16 v148, v157
	v_mov_b32_e32 v192, v106
	v_mov_b32_e32 v193, v110
	v_mul_f32 v136, -2.0, v137
	s_nop 6
	ds_read_b128 v[208:211], v139
	s_waitcnt lgkmcnt(1)
	s_barrier
	ds_read_b128 v[212:215], v140
	ds_read_b128 v[216:219], v141
	s_waitcnt lgkmcnt(2)
	v_smfmac_f32_16x16x64_f16 v[192:195], v[208:211], v[6:13], v191
	ds_read_b128 v[220:223], v142
	s_waitcnt lgkmcnt(2)
	v_smfmac_f32_16x16x64_f16 v[192:195], v[212:215], v[14:21], v191
	s_waitcnt lgkmcnt(1)
	v_smfmac_f32_16x16x64_f16 v[192:195], v[216:219], v[26:33], v191
	s_waitcnt lgkmcnt(0)
	v_smfmac_f32_16x16x64_f16 v[192:195], v[220:223], v[34:41], v191
	s_nop 7
	v_cndmask_b32_e64 v156, v192, v193, s[0:1]
	v_exp_f32_e64 v158, -|v156|
	v_max_f32 v159, 0, v156
	v_add_f32 v158, 1.0, v158
	v_log_f32 v158, v158
	s_nop 0
	v_fma_mixlo_f16 v157, v158, 1.0, v159
	ds_write_b16 v149, v157
	v_mov_b32_e32 v200, v114
	v_mov_b32_e32 v201, v118
	v_mov_b32_e32 v204, v122
	v_mov_b32_e32 v205, v126
	s_nop 3
	ds_read_b128 v[208:211], v143
	s_waitcnt lgkmcnt(1)
	s_barrier
	ds_read_b128 v[212:215], v144
	ds_read_b128 v[216:219], v145
	s_waitcnt lgkmcnt(2)
	v_smfmac_f32_16x16x64_f16 v[200:203], v[208:211], v[42:49], v191
	v_smfmac_f32_16x16x64_f16 v[204:207], v[208:211], v[74:81], v191
	ds_read_b128 v[220:223], v146
	s_waitcnt lgkmcnt(2)
	v_smfmac_f32_16x16x64_f16 v[200:203], v[212:215], v[50:57], v191
	v_smfmac_f32_16x16x64_f16 v[204:207], v[212:215], v[82:89], v191
	s_waitcnt lgkmcnt(1)
	v_smfmac_f32_16x16x64_f16 v[200:203], v[216:219], v[58:65], v191
	v_smfmac_f32_16x16x64_f16 v[204:207], v[216:219], v[90:97], v191
	s_waitcnt lgkmcnt(0)
	v_smfmac_f32_16x16x64_f16 v[200:203], v[220:223], v[66:73], v191
	v_smfmac_f32_16x16x64_f16 v[204:207], v[220:223], v[98:105], v191
	s_nop 6
	v_cndmask_b32_e64 v172, v201, v200, s[6:7]
	v_cndmask_b32_e64 v172, v172, v204, s[0:1]
	v_cndmask_b32_e64 v172, v172, v205, s[4:5]
	v_exp_f32_e32 v172, v172
	s_nop 0
	v_add_f32_e32 v172, 1.0, v172
	v_rcp_f32_e32 v172, v172
	s_nop 0
	v_fmac_f32_e32 v137, v172, v136
	s_nop 1
	v_add_f32_dpp v136, v137, v137 quad_perm:[1,0,3,2] row_mask:0xf bank_mask:0xf bound_ctrl:1
	s_nop 1
	v_add_f32_dpp v136, v136, v136 quad_perm:[2,3,0,1] row_mask:0xf bank_mask:0xf bound_ctrl:1
	s_nop 1
	v_add_f32_dpp v136, v136, v136 row_half_mirror row_mask:0xf bank_mask:0xf bound_ctrl:1
	v_cvt_f16_f32_e32 v137, v136
	ds_write_b16 v150, v137
	s_waitcnt lgkmcnt(0)
	s_barrier
	ds_read_b128 v[156:159], v147
	s_nop 3
	ds_read_b32 v137, v134 offset:160
	v_add_f32_e32 v135, v135, v136
	s_waitcnt lgkmcnt(1)
	v_smfmac_f32_16x16x64_f16 v[130:133], v[156:159], v[248:255], v191
	s_nop 7
	v_cndmask_b32_e64 v156, v130, v131, s[0:1]
	v_exp_f32_e64 v158, -|v156|
	v_max_f32 v159, 0, v156
	v_add_f32 v158, 1.0, v158
	v_log_f32 v158, v158
	s_nop 0
	v_fma_mixlo_f16 v157, v158, 1.0, v159
	ds_write_b16 v148, v157
	v_mov_b32_e32 v192, v106
	v_mov_b32_e32 v193, v110
	v_mul_f32 v136, -2.0, v137
	s_nop 6
	ds_read_b128 v[208:211], v139
	s_waitcnt lgkmcnt(1)
	s_barrier
	ds_read_b128 v[212:215], v140
	ds_read_b128 v[216:219], v141
	s_waitcnt lgkmcnt(2)
	v_smfmac_f32_16x16x64_f16 v[192:195], v[208:211], v[6:13], v191
	ds_read_b128 v[220:223], v142
	s_waitcnt lgkmcnt(2)
	v_smfmac_f32_16x16x64_f16 v[192:195], v[212:215], v[14:21], v191
	s_waitcnt lgkmcnt(1)
	v_smfmac_f32_16x16x64_f16 v[192:195], v[216:219], v[26:33], v191
	s_waitcnt lgkmcnt(0)
	v_smfmac_f32_16x16x64_f16 v[192:195], v[220:223], v[34:41], v191
	s_nop 7
	v_cndmask_b32_e64 v156, v192, v193, s[0:1]
	v_exp_f32_e64 v158, -|v156|
	v_max_f32 v159, 0, v156
	v_add_f32 v158, 1.0, v158
	v_log_f32 v158, v158
	s_nop 0
	v_fma_mixlo_f16 v157, v158, 1.0, v159
	ds_write_b16 v149, v157
	v_mov_b32_e32 v200, v114
	v_mov_b32_e32 v201, v118
	v_mov_b32_e32 v204, v122
	v_mov_b32_e32 v205, v126
	s_nop 3
	ds_read_b128 v[208:211], v143
	s_waitcnt lgkmcnt(1)
	s_barrier
	ds_read_b128 v[212:215], v144
	ds_read_b128 v[216:219], v145
	s_waitcnt lgkmcnt(2)
	v_smfmac_f32_16x16x64_f16 v[200:203], v[208:211], v[42:49], v191
	v_smfmac_f32_16x16x64_f16 v[204:207], v[208:211], v[74:81], v191
	ds_read_b128 v[220:223], v146
	s_waitcnt lgkmcnt(2)
	v_smfmac_f32_16x16x64_f16 v[200:203], v[212:215], v[50:57], v191
	v_smfmac_f32_16x16x64_f16 v[204:207], v[212:215], v[82:89], v191
	s_waitcnt lgkmcnt(1)
	v_smfmac_f32_16x16x64_f16 v[200:203], v[216:219], v[58:65], v191
	v_smfmac_f32_16x16x64_f16 v[204:207], v[216:219], v[90:97], v191
	s_waitcnt lgkmcnt(0)
	v_smfmac_f32_16x16x64_f16 v[200:203], v[220:223], v[66:73], v191
	v_smfmac_f32_16x16x64_f16 v[204:207], v[220:223], v[98:105], v191
	s_nop 6
	v_cndmask_b32_e64 v172, v201, v200, s[6:7]
	v_cndmask_b32_e64 v172, v172, v204, s[0:1]
	v_cndmask_b32_e64 v172, v172, v205, s[4:5]
	v_exp_f32_e32 v172, v172
	s_nop 0
	v_add_f32_e32 v172, 1.0, v172
	v_rcp_f32_e32 v172, v172
	s_nop 0
	v_fmac_f32_e32 v137, v172, v136
	s_nop 1
	v_add_f32_dpp v136, v137, v137 quad_perm:[1,0,3,2] row_mask:0xf bank_mask:0xf bound_ctrl:1
	s_nop 1
	v_add_f32_dpp v136, v136, v136 quad_perm:[2,3,0,1] row_mask:0xf bank_mask:0xf bound_ctrl:1
	s_nop 1
	v_add_f32_dpp v136, v136, v136 row_half_mirror row_mask:0xf bank_mask:0xf bound_ctrl:1
	v_cvt_f16_f32_e32 v137, v136
	ds_write_b16 v150, v137
	s_waitcnt lgkmcnt(0)
	s_barrier
	ds_read_b128 v[156:159], v147
	s_nop 3
	ds_read_b32 v137, v134 offset:192
	v_add_f32_e32 v135, v135, v136
	s_waitcnt lgkmcnt(1)
	v_smfmac_f32_16x16x64_f16 v[130:133], v[156:159], v[248:255], v191
	s_nop 7
	v_cndmask_b32_e64 v152, v130, v131, s[0:1]
	v_exp_f32_e64 v158, -|v152|
	v_max_f32 v159, 0, v152
	v_add_f32 v158, 1.0, v158
	v_log_f32 v158, v158
	s_nop 0
	v_fma_mixlo_f16 v153, v158, 1.0, v159
	ds_write_b16 v148, v153
	v_mov_b32_e32 v192, v106
	v_mov_b32_e32 v193, v110
	v_mul_f32 v136, -2.0, v137
	s_nop 6
	ds_read_b128 v[208:211], v139
	s_waitcnt lgkmcnt(1)
	s_barrier
	ds_read_b128 v[212:215], v140
	ds_read_b128 v[216:219], v141
	s_waitcnt lgkmcnt(2)
	v_smfmac_f32_16x16x64_f16 v[192:195], v[208:211], v[6:13], v191
	ds_read_b128 v[220:223], v142
	s_waitcnt lgkmcnt(2)
	v_smfmac_f32_16x16x64_f16 v[192:195], v[212:215], v[14:21], v191
	s_waitcnt lgkmcnt(1)
	v_smfmac_f32_16x16x64_f16 v[192:195], v[216:219], v[26:33], v191
	s_waitcnt lgkmcnt(0)
	v_smfmac_f32_16x16x64_f16 v[192:195], v[220:223], v[34:41], v191
	s_nop 7
	v_cndmask_b32_e64 v152, v192, v193, s[0:1]
	v_exp_f32_e64 v158, -|v152|
	v_max_f32 v159, 0, v152
	v_add_f32 v158, 1.0, v158
	v_log_f32 v158, v158
	s_nop 0
	v_fma_mixlo_f16 v153, v158, 1.0, v159
	ds_write_b16 v149, v153
	v_mov_b32_e32 v200, v114
	v_mov_b32_e32 v201, v118
	v_mov_b32_e32 v204, v122
	v_mov_b32_e32 v205, v126
	s_nop 3
	ds_read_b128 v[208:211], v143
	s_waitcnt lgkmcnt(1)
	s_barrier
	ds_read_b128 v[212:215], v144
	ds_read_b128 v[216:219], v145
	s_waitcnt lgkmcnt(2)
	v_smfmac_f32_16x16x64_f16 v[200:203], v[208:211], v[42:49], v191
	v_smfmac_f32_16x16x64_f16 v[204:207], v[208:211], v[74:81], v191
	ds_read_b128 v[220:223], v146
	s_waitcnt lgkmcnt(2)
	v_smfmac_f32_16x16x64_f16 v[200:203], v[212:215], v[50:57], v191
	v_smfmac_f32_16x16x64_f16 v[204:207], v[212:215], v[82:89], v191
	s_waitcnt lgkmcnt(1)
	v_smfmac_f32_16x16x64_f16 v[200:203], v[216:219], v[58:65], v191
	v_smfmac_f32_16x16x64_f16 v[204:207], v[216:219], v[90:97], v191
	s_waitcnt lgkmcnt(0)
	v_smfmac_f32_16x16x64_f16 v[200:203], v[220:223], v[66:73], v191
	v_smfmac_f32_16x16x64_f16 v[204:207], v[220:223], v[98:105], v191
	s_nop 6
	v_cndmask_b32_e64 v152, v201, v200, s[6:7]
	v_cndmask_b32_e64 v152, v152, v204, s[0:1]
	v_cndmask_b32_e64 v152, v152, v205, s[4:5]
	v_exp_f32_e32 v152, v152
	s_nop 0
	v_add_f32_e32 v152, 1.0, v152
	v_rcp_f32_e32 v152, v152
	s_nop 0
	v_fmac_f32_e32 v137, v152, v136
	s_nop 1
	v_add_f32_dpp v136, v137, v137 quad_perm:[1,0,3,2] row_mask:0xf bank_mask:0xf bound_ctrl:1
	s_nop 1
	v_add_f32_dpp v136, v136, v136 quad_perm:[2,3,0,1] row_mask:0xf bank_mask:0xf bound_ctrl:1
	s_nop 1
	v_add_f32_dpp v136, v136, v136 row_half_mirror row_mask:0xf bank_mask:0xf bound_ctrl:1
	v_cvt_f16_f32_e32 v137, v136
	ds_write_b16 v150, v137
	s_waitcnt lgkmcnt(0)
	s_barrier
	ds_read_b128 v[158:161], v147
	v_add_f32_e32 v152, v135, v136
	ds_read_b32 v153, v134 offset:224
	s_addk_i32 s3, 0x100
	s_cmpk_eq_u32 s3, 0xfa20
	s_waitcnt lgkmcnt(1)
	v_smfmac_f32_16x16x64_f16 v[130:133], v[158:161], v[248:255], v191
	s_nop 7
	v_cndmask_b32_e64 v154, v130, v131, s[0:1]
	s_cbranch_scc0 .LBB0_21
	s_and_saveexec_b64 s[0:1], vcc
	ds_write_b32 v1, v152
	s_or_b64 exec, exec, s[0:1]
	v_cmp_gt_u32_e32 vcc, 10, v0
	s_waitcnt lgkmcnt(0)
	s_barrier
	s_and_saveexec_b64 s[0:1], vcc
	s_cbranch_execz .LBB0_28
	v_lshlrev_b32_e32 v1, 2, v0
	global_load_dword v1, v1, s[12:13]
	v_mov_b32_e32 v139, 0
	v_lshl_add_u64 v[2:3], s[10:11], 0, v[138:139]
	v_lshl_add_u64 v[2:3], v[2:3], 0, 28
	s_mov_b32 s0, 0
